# k_bucket_sort scatter in 2 passes (quarters 0/1 allocated upwards from row start, 3/2 downwards from row end, one LDS atomic per edge and pass) instead of 4; hop gather addresses masked again
# speedup vs baseline: 1.0059x; 1.0059x over previous
.LBB2_108:
	s_and_b64 vcc, exec, s[0:1]
	s_cbranch_vccz .LBB2_129
	s_mov_b32 s58, 0x29f17
	v_lshlrev_b32_e32 v81, 2, v0
	v_add_u32_e32 v82, 0x10004, v81
	ds_read_b32 v83, v82
	s_sub_i32 s93, s37, s46
	v_mov_b32_e32 v84, s93
	v_and_b32_e32 v64, 0x1ffff, v30
	v_mul_hi_u32 v64, v64, s58
	v_cmp_lt_u32_e32 vcc, 1, v64
	v_cndmask_b32_e64 v97, 1, -1, vcc
	v_and_b32_e32 v65, 0x1ffff, v32
	v_mul_hi_u32 v65, v65, s58
	v_cmp_lt_u32_e32 vcc, 1, v65
	v_cndmask_b32_e64 v98, 1, -1, vcc
	v_and_b32_e32 v66, 0x1ffff, v18
	v_mul_hi_u32 v66, v66, s58
	v_cmp_lt_u32_e32 vcc, 1, v66
	v_cndmask_b32_e64 v99, 1, -1, vcc
	v_and_b32_e32 v67, 0x1ffff, v20
	v_mul_hi_u32 v67, v67, s58
	v_cmp_lt_u32_e32 vcc, 1, v67
	v_cndmask_b32_e64 v100, 1, -1, vcc
	v_and_b32_e32 v68, 0x1ffff, v26
	v_mul_hi_u32 v68, v68, s58
	v_cmp_lt_u32_e32 vcc, 1, v68
	v_cndmask_b32_e64 v101, 1, -1, vcc
	v_and_b32_e32 v69, 0x1ffff, v28
	v_mul_hi_u32 v69, v69, s58
	v_cmp_lt_u32_e32 vcc, 1, v69
	v_cndmask_b32_e64 v102, 1, -1, vcc
	v_and_b32_e32 v70, 0x1ffff, v10
	v_mul_hi_u32 v70, v70, s58
	v_cmp_lt_u32_e32 vcc, 1, v70
	v_cndmask_b32_e64 v103, 1, -1, vcc
	v_and_b32_e32 v71, 0x1ffff, v12
	v_mul_hi_u32 v71, v71, s58
	v_cmp_lt_u32_e32 vcc, 1, v71
	v_cndmask_b32_e64 v104, 1, -1, vcc
	v_and_b32_e32 v72, 0x1ffff, v22
	v_mul_hi_u32 v72, v72, s58
	v_cmp_lt_u32_e32 vcc, 1, v72
	v_cndmask_b32_e64 v105, 1, -1, vcc
	v_and_b32_e32 v73, 0x1ffff, v24
	v_mul_hi_u32 v73, v73, s58
	v_cmp_lt_u32_e32 vcc, 1, v73
	v_cndmask_b32_e64 v106, 1, -1, vcc
	v_and_b32_e32 v74, 0x1ffff, v6
	v_mul_hi_u32 v74, v74, s58
	v_cmp_lt_u32_e32 vcc, 1, v74
	v_cndmask_b32_e64 v107, 1, -1, vcc
	v_and_b32_e32 v75, 0x1ffff, v8
	v_mul_hi_u32 v75, v75, s58
	v_cmp_lt_u32_e32 vcc, 1, v75
	v_cndmask_b32_e64 v108, 1, -1, vcc
	v_and_b32_e32 v76, 0x1ffff, v14
	v_mul_hi_u32 v76, v76, s58
	v_cmp_lt_u32_e32 vcc, 1, v76
	v_cndmask_b32_e64 v109, 1, -1, vcc
	v_and_b32_e32 v77, 0x1ffff, v16
	v_mul_hi_u32 v77, v77, s58
	v_cmp_lt_u32_e32 vcc, 1, v77
	v_cndmask_b32_e64 v110, 1, -1, vcc
	v_and_b32_e32 v78, 0x1ffff, v2
	v_mul_hi_u32 v78, v78, s58
	v_cmp_lt_u32_e32 vcc, 1, v78
	v_cndmask_b32_e64 v111, 1, -1, vcc
	v_and_b32_e32 v79, 0x1ffff, v4
	v_mul_hi_u32 v79, v79, s58
	v_cmp_lt_u32_e32 vcc, 1, v79
	v_cndmask_b32_e64 v112, 1, -1, vcc
	v_cmp_eq_u32_e32 vcc, 0x1ff, v0
	s_waitcnt lgkmcnt(0)
	v_cndmask_b32_e32 v83, v83, v84, vcc
	v_add_u32_e32 v82, 0x10840, v81
	ds_write_b32 v82, v83
	s_mov_b32 s92, 0x10000
	s_waitcnt lgkmcnt(0)
	s_barrier
	s_mov_b32 s59, 0
	s_mov_b32 s58, 3
.Lk3_pass:
	v_cmp_eq_u32_e64 s[60:61], s59, v64
	v_cmp_eq_u32_e32 vcc, s58, v64
	s_or_b64 s[60:61], s[60:61], vcc
	s_and_b64 s[60:61], s[60:61], s[30:31]
	v_cmp_eq_u32_e64 s[62:63], s59, v65
	v_cmp_eq_u32_e32 vcc, s58, v65
	s_or_b64 s[62:63], s[62:63], vcc
	s_and_b64 s[62:63], s[62:63], s[28:29]
	v_cmp_eq_u32_e64 s[64:65], s59, v66
	v_cmp_eq_u32_e32 vcc, s58, v66
	s_or_b64 s[64:65], s[64:65], vcc
	s_and_b64 s[64:65], s[64:65], s[26:27]
	v_cmp_eq_u32_e64 s[66:67], s59, v67
	v_cmp_eq_u32_e32 vcc, s58, v67
	s_or_b64 s[66:67], s[66:67], vcc
	s_and_b64 s[66:67], s[66:67], s[24:25]
	v_cmp_eq_u32_e64 s[68:69], s59, v68
	v_cmp_eq_u32_e32 vcc, s58, v68
	s_or_b64 s[68:69], s[68:69], vcc
	s_and_b64 s[68:69], s[68:69], s[22:23]
	v_cmp_eq_u32_e64 s[70:71], s59, v69
	v_cmp_eq_u32_e32 vcc, s58, v69
	s_or_b64 s[70:71], s[70:71], vcc
	s_and_b64 s[70:71], s[70:71], s[20:21]
	v_cmp_eq_u32_e64 s[72:73], s59, v70
	v_cmp_eq_u32_e32 vcc, s58, v70
	s_or_b64 s[72:73], s[72:73], vcc
	s_and_b64 s[72:73], s[72:73], s[18:19]
	v_cmp_eq_u32_e64 s[74:75], s59, v71
	v_cmp_eq_u32_e32 vcc, s58, v71
	s_or_b64 s[74:75], s[74:75], vcc
	s_and_b64 s[74:75], s[74:75], s[16:17]
	v_cmp_eq_u32_e64 s[76:77], s59, v72
	v_cmp_eq_u32_e32 vcc, s58, v72
	s_or_b64 s[76:77], s[76:77], vcc
	s_and_b64 s[76:77], s[76:77], s[14:15]
	v_cmp_eq_u32_e64 s[78:79], s59, v73
	v_cmp_eq_u32_e32 vcc, s58, v73
	s_or_b64 s[78:79], s[78:79], vcc
	s_and_b64 s[78:79], s[78:79], s[12:13]
	v_cmp_eq_u32_e64 s[80:81], s59, v74
	v_cmp_eq_u32_e32 vcc, s58, v74
	s_or_b64 s[80:81], s[80:81], vcc
	s_and_b64 s[80:81], s[80:81], s[10:11]
	v_cmp_eq_u32_e64 s[82:83], s59, v75
	v_cmp_eq_u32_e32 vcc, s58, v75
	s_or_b64 s[82:83], s[82:83], vcc
	s_and_b64 s[82:83], s[82:83], s[8:9]
	v_cmp_eq_u32_e64 s[84:85], s59, v76
	v_cmp_eq_u32_e32 vcc, s58, v76
	s_or_b64 s[84:85], s[84:85], vcc
	s_and_b64 s[84:85], s[84:85], s[6:7]
	v_cmp_eq_u32_e64 s[86:87], s59, v77
	v_cmp_eq_u32_e32 vcc, s58, v77
	s_or_b64 s[86:87], s[86:87], vcc
	s_and_b64 s[86:87], s[86:87], s[4:5]
	v_cmp_eq_u32_e64 s[88:89], s59, v78
	v_cmp_eq_u32_e32 vcc, s58, v78
	s_or_b64 s[88:89], s[88:89], vcc
	s_and_b64 s[88:89], s[88:89], s[2:3]
	v_cmp_eq_u32_e64 s[90:91], s59, v79
	v_cmp_eq_u32_e32 vcc, s58, v79
	s_or_b64 s[90:91], s[90:91], vcc
	s_and_b64 s[90:91], s[90:91], s[34:35]
	s_mov_b64 exec, s[60:61]
	v_lshrrev_b32_e32 v48, 15, v30
	v_and_b32_e32 v48, 0x1fffc, v48
	v_and_b32_e32 v81, 0x840, v97
	v_add3_u32 v48, v48, v81, s92
	ds_add_rtn_u32 v48, v48, v97
	s_mov_b64 exec, s[62:63]
	v_lshrrev_b32_e32 v49, 15, v32
	v_and_b32_e32 v49, 0x1fffc, v49
	v_and_b32_e32 v81, 0x840, v98
	v_add3_u32 v49, v49, v81, s92
	ds_add_rtn_u32 v49, v49, v98
	s_mov_b64 exec, s[64:65]
	v_lshrrev_b32_e32 v50, 15, v18
	v_and_b32_e32 v50, 0x1fffc, v50
	v_and_b32_e32 v81, 0x840, v99
	v_add3_u32 v50, v50, v81, s92
	ds_add_rtn_u32 v50, v50, v99
	s_mov_b64 exec, s[66:67]
	v_lshrrev_b32_e32 v51, 15, v20
	v_and_b32_e32 v51, 0x1fffc, v51
	v_and_b32_e32 v81, 0x840, v100
	v_add3_u32 v51, v51, v81, s92
	ds_add_rtn_u32 v51, v51, v100
	s_mov_b64 exec, s[68:69]
	v_lshrrev_b32_e32 v52, 15, v26
	v_and_b32_e32 v52, 0x1fffc, v52
	v_and_b32_e32 v81, 0x840, v101
	v_add3_u32 v52, v52, v81, s92
	ds_add_rtn_u32 v52, v52, v101
	s_mov_b64 exec, s[70:71]
	v_lshrrev_b32_e32 v53, 15, v28
	v_and_b32_e32 v53, 0x1fffc, v53
	v_and_b32_e32 v81, 0x840, v102
	v_add3_u32 v53, v53, v81, s92
	ds_add_rtn_u32 v53, v53, v102
	s_mov_b64 exec, s[72:73]
	v_lshrrev_b32_e32 v54, 15, v10
	v_and_b32_e32 v54, 0x1fffc, v54
	v_and_b32_e32 v81, 0x840, v103
	v_add3_u32 v54, v54, v81, s92
	ds_add_rtn_u32 v54, v54, v103
	s_mov_b64 exec, s[74:75]
	v_lshrrev_b32_e32 v55, 15, v12
	v_and_b32_e32 v55, 0x1fffc, v55
	v_and_b32_e32 v81, 0x840, v104
	v_add3_u32 v55, v55, v81, s92
	ds_add_rtn_u32 v55, v55, v104
	s_mov_b64 exec, s[76:77]
	v_lshrrev_b32_e32 v56, 15, v22
	v_and_b32_e32 v56, 0x1fffc, v56
	v_and_b32_e32 v81, 0x840, v105
	v_add3_u32 v56, v56, v81, s92
	ds_add_rtn_u32 v56, v56, v105
	s_mov_b64 exec, s[78:79]
	v_lshrrev_b32_e32 v57, 15, v24
	v_and_b32_e32 v57, 0x1fffc, v57
	v_and_b32_e32 v81, 0x840, v106
	v_add3_u32 v57, v57, v81, s92
	ds_add_rtn_u32 v57, v57, v106
	s_mov_b64 exec, s[80:81]
	v_lshrrev_b32_e32 v58, 15, v6
	v_and_b32_e32 v58, 0x1fffc, v58
	v_and_b32_e32 v81, 0x840, v107
	v_add3_u32 v58, v58, v81, s92
	ds_add_rtn_u32 v58, v58, v107
	s_mov_b64 exec, s[82:83]
	v_lshrrev_b32_e32 v59, 15, v8
	v_and_b32_e32 v59, 0x1fffc, v59
	v_and_b32_e32 v81, 0x840, v108
	v_add3_u32 v59, v59, v81, s92
	ds_add_rtn_u32 v59, v59, v108
	s_waitcnt lgkmcnt(8)
	s_mov_b64 exec, s[84:85]
	v_lshrrev_b32_e32 v60, 15, v14
	v_and_b32_e32 v60, 0x1fffc, v60
	v_and_b32_e32 v81, 0x840, v109
	v_add3_u32 v60, v60, v81, s92
	ds_add_rtn_u32 v60, v60, v109
	s_mov_b64 exec, s[86:87]
	v_lshrrev_b32_e32 v61, 15, v16
	v_and_b32_e32 v61, 0x1fffc, v61
	v_and_b32_e32 v81, 0x840, v110
	v_add3_u32 v61, v61, v81, s92
	ds_add_rtn_u32 v61, v61, v110
	s_mov_b64 exec, s[88:89]
	v_lshrrev_b32_e32 v62, 15, v2
	v_and_b32_e32 v62, 0x1fffc, v62
	v_and_b32_e32 v81, 0x840, v111
	v_add3_u32 v62, v62, v81, s92
	ds_add_rtn_u32 v62, v62, v111
	s_mov_b64 exec, s[90:91]
	v_lshrrev_b32_e32 v63, 15, v4
	v_and_b32_e32 v63, 0x1fffc, v63
	v_and_b32_e32 v81, 0x840, v112
	v_add3_u32 v63, v63, v81, s92
	ds_add_rtn_u32 v63, v63, v112
	s_waitcnt lgkmcnt(0)
	s_mov_b64 exec, s[60:61]
	v_ashrrev_i32_e32 v81, 1, v97
	v_and_b32_e32 v30, 0x1ffff, v30
	v_add_lshl_u32 v48, v48, v81, 3
	ds_write_b64 v48, v[30:31]
	s_mov_b64 exec, s[62:63]
	v_ashrrev_i32_e32 v81, 1, v98
	v_and_b32_e32 v32, 0x1ffff, v32
	v_add_lshl_u32 v49, v49, v81, 3
	ds_write_b64 v49, v[32:33]
	s_mov_b64 exec, s[64:65]
	v_ashrrev_i32_e32 v81, 1, v99
	v_and_b32_e32 v18, 0x1ffff, v18
	v_add_lshl_u32 v50, v50, v81, 3
	ds_write_b64 v50, v[18:19]
	s_mov_b64 exec, s[66:67]
	v_ashrrev_i32_e32 v81, 1, v100
	v_and_b32_e32 v20, 0x1ffff, v20
	v_add_lshl_u32 v51, v51, v81, 3
	ds_write_b64 v51, v[20:21]
	s_mov_b64 exec, s[68:69]
	v_ashrrev_i32_e32 v81, 1, v101
	v_and_b32_e32 v26, 0x1ffff, v26
	v_add_lshl_u32 v52, v52, v81, 3
	ds_write_b64 v52, v[26:27]
	s_mov_b64 exec, s[70:71]
	v_ashrrev_i32_e32 v81, 1, v102
	v_and_b32_e32 v28, 0x1ffff, v28
	v_add_lshl_u32 v53, v53, v81, 3
	ds_write_b64 v53, v[28:29]
	s_mov_b64 exec, s[72:73]
	v_ashrrev_i32_e32 v81, 1, v103
	v_and_b32_e32 v10, 0x1ffff, v10
	v_add_lshl_u32 v54, v54, v81, 3
	ds_write_b64 v54, v[10:11]
	s_mov_b64 exec, s[74:75]
	v_ashrrev_i32_e32 v81, 1, v104
	v_and_b32_e32 v12, 0x1ffff, v12
	v_add_lshl_u32 v55, v55, v81, 3
	ds_write_b64 v55, v[12:13]
	s_mov_b64 exec, s[76:77]
	v_ashrrev_i32_e32 v81, 1, v105
	v_and_b32_e32 v22, 0x1ffff, v22
	v_add_lshl_u32 v56, v56, v81, 3
	ds_write_b64 v56, v[22:23]
	s_mov_b64 exec, s[78:79]
	v_ashrrev_i32_e32 v81, 1, v106
	v_and_b32_e32 v24, 0x1ffff, v24
	v_add_lshl_u32 v57, v57, v81, 3
	ds_write_b64 v57, v[24:25]
	s_mov_b64 exec, s[80:81]
	v_ashrrev_i32_e32 v81, 1, v107
	v_and_b32_e32 v6, 0x1ffff, v6
	v_add_lshl_u32 v58, v58, v81, 3
	ds_write_b64 v58, v[6:7]
	s_mov_b64 exec, s[82:83]
	v_ashrrev_i32_e32 v81, 1, v108
	v_and_b32_e32 v8, 0x1ffff, v8
	v_add_lshl_u32 v59, v59, v81, 3
	ds_write_b64 v59, v[8:9]
	s_waitcnt lgkmcnt(8)
	s_mov_b64 exec, s[84:85]
	v_ashrrev_i32_e32 v81, 1, v109
	v_and_b32_e32 v14, 0x1ffff, v14
	v_add_lshl_u32 v60, v60, v81, 3
	ds_write_b64 v60, v[14:15]
	s_mov_b64 exec, s[86:87]
	v_ashrrev_i32_e32 v81, 1, v110
	v_and_b32_e32 v16, 0x1ffff, v16
	v_add_lshl_u32 v61, v61, v81, 3
	ds_write_b64 v61, v[16:17]
	s_mov_b64 exec, s[88:89]
	v_ashrrev_i32_e32 v81, 1, v111
	v_and_b32_e32 v2, 0x1ffff, v2
	v_add_lshl_u32 v62, v62, v81, 3
	ds_write_b64 v62, v[2:3]
	s_mov_b64 exec, s[90:91]
	v_ashrrev_i32_e32 v81, 1, v112
	v_and_b32_e32 v4, 0x1ffff, v4
	v_add_lshl_u32 v63, v63, v81, 3
	ds_write_b64 v63, v[4:5]
	s_mov_b64 exec, -1
	s_waitcnt lgkmcnt(0)
	s_barrier
	s_add_i32 s59, s59, 1
	s_sub_i32 s58, s58, 1
	s_cmp_lt_u32 s59, 2
	s_cbranch_scc1 .Lk3_pass

	.amdhsa_kernel _Z13k_bucket_sortPKiPK15HIP_vector_typeIiLj2EEPiPS2_
		.amdhsa_group_segment_fixed_size 69696
		.amdhsa_private_segment_fixed_size 0
		.amdhsa_kernarg_size 32
		.amdhsa_user_sgpr_count 2
		.amdhsa_user_sgpr_dispatch_ptr 0
		.amdhsa_user_sgpr_queue_ptr 0
		.amdhsa_user_sgpr_kernarg_segment_ptr 1
		.amdhsa_user_sgpr_dispatch_id 0
		.amdhsa_user_sgpr_kernarg_preload_length 0
		.amdhsa_user_sgpr_kernarg_preload_offset 0
		.amdhsa_user_sgpr_private_segment_size 0
		.amdhsa_uses_dynamic_stack 0
		.amdhsa_enable_private_segment 0
		.amdhsa_system_sgpr_workgroup_id_x 1
		.amdhsa_system_sgpr_workgroup_id_y 0
		.amdhsa_system_sgpr_workgroup_id_z 0
		.amdhsa_system_sgpr_workgroup_info 0
		.amdhsa_system_vgpr_workitem_id 0
		.amdhsa_next_free_vgpr 120
		.amdhsa_next_free_sgpr 96
		.amdhsa_accum_offset 120
		.amdhsa_reserve_vcc 1
		.amdhsa_float_round_mode_32 0
		.amdhsa_float_round_mode_16_64 0
		.amdhsa_float_denorm_mode_32 3
		.amdhsa_float_denorm_mode_16_64 3
		.amdhsa_dx10_clamp 1
		.amdhsa_ieee_mode 1
		.amdhsa_fp16_overflow 0
		.amdhsa_tg_split 0
		.amdhsa_exception_fp_ieee_invalid_op 0
		.amdhsa_exception_fp_denorm_src 0
		.amdhsa_exception_fp_ieee_div_zero 0
		.amdhsa_exception_fp_ieee_overflow 0
		.amdhsa_exception_fp_ieee_underflow 0
		.amdhsa_exception_fp_ieee_inexact 0
		.amdhsa_exception_int_div_zero 0
	.end_amdhsa_kernel

amdhsa.kernels:
  - .agpr_count:     0
    .args:
      - .actual_access:  read_only
        .address_space:  global
        .offset:         0
        .size:           8
        .value_kind:     global_buffer
      - .actual_access:  read_only
        .address_space:  global
        .offset:         8
        .size:           8
        .value_kind:     global_buffer
      - .actual_access:  read_only
        .address_space:  global
        .offset:         16
        .size:           8
        .value_kind:     global_buffer
      - .actual_access:  read_only
        .address_space:  global
        .offset:         24
        .size:           8
        .value_kind:     global_buffer
      - .actual_access:  write_only
        .address_space:  global
        .offset:         32
        .size:           8
        .value_kind:     global_buffer
      - .actual_access:  write_only
        .address_space:  global
        .offset:         40
        .size:           8
        .value_kind:     global_buffer
    .group_segment_fixed_size: 784
    .kernarg_segment_align: 8
    .kernarg_segment_size: 48
    .language:       OpenCL C
    .language_version:
      - 2
      - 0
    .max_flat_workgroup_size: 256
    .name:           _Z14k_hist_convertPKiS0_PKfS2_PiP15HIP_vector_typeIjLj4EE
    .private_segment_fixed_size: 0
    .sgpr_count:     18
    .sgpr_spill_count: 0
    .symbol:         _Z14k_hist_convertPKiS0_PKfS2_PiP15HIP_vector_typeIjLj4EE.kd
    .uniform_work_group_size: 1
    .uses_dynamic_stack: false
    .vgpr_count:     43
    .vgpr_spill_count: 0
    .wavefront_size: 64
  - .agpr_count:     0
    .args:
      - .actual_access:  read_only
        .address_space:  global
        .offset:         0
        .size:           8
        .value_kind:     global_buffer
      - .actual_access:  read_only
        .address_space:  global
        .offset:         8
        .size:           8
        .value_kind:     global_buffer
      - .actual_access:  read_only
        .address_space:  global
        .offset:         16
        .size:           8
        .value_kind:     global_buffer
      - .actual_access:  read_only
        .address_space:  global
        .offset:         24
        .size:           8
        .value_kind:     global_buffer
      - .actual_access:  read_only
        .address_space:  global
        .offset:         32
        .size:           8
        .value_kind:     global_buffer
      - .actual_access:  read_only
        .address_space:  global
        .offset:         40
        .size:           8
        .value_kind:     global_buffer
      - .actual_access:  read_only
        .address_space:  global
        .offset:         48
        .size:           8
        .value_kind:     global_buffer
      - .actual_access:  write_only
        .address_space:  global
        .offset:         56
        .size:           8
        .value_kind:     global_buffer
      - .actual_access:  write_only
        .address_space:  global
        .offset:         64
        .size:           8
        .value_kind:     global_buffer
    .group_segment_fixed_size: 90432
    .kernarg_segment_align: 8
    .kernarg_segment_size: 72
    .language:       OpenCL C
    .language_version:
      - 2
      - 0
    .max_flat_workgroup_size: 1024
    .name:           _Z16k_bucket_scatterPKiS0_PKfS0_S0_S2_S0_PiP15HIP_vector_typeIiLj2EE
    .private_segment_fixed_size: 0
    .sgpr_count:     30
    .sgpr_spill_count: 0
    .symbol:         _Z16k_bucket_scatterPKiS0_PKfS0_S0_S2_S0_PiP15HIP_vector_typeIiLj2EE.kd
    .uniform_work_group_size: 1
    .uses_dynamic_stack: false
    .vgpr_count:     77
    .vgpr_spill_count: 0
    .wavefront_size: 64
  - .agpr_count:     0
    .args:
      - .actual_access:  read_only
        .address_space:  global
        .offset:         0
        .size:           8
        .value_kind:     global_buffer
      - .actual_access:  read_only
        .address_space:  global
        .offset:         8
        .size:           8
        .value_kind:     global_buffer
      - .actual_access:  write_only
        .address_space:  global
        .offset:         16
        .size:           8
        .value_kind:     global_buffer
      - .actual_access:  write_only
        .address_space:  global
        .offset:         24
        .size:           8
        .value_kind:     global_buffer
    .group_segment_fixed_size: 69696
    .kernarg_segment_align: 8
    .kernarg_segment_size: 32
    .language:       OpenCL C
    .language_version:
      - 2
      - 0
    .max_flat_workgroup_size: 512
    .name:           _Z13k_bucket_sortPKiPK15HIP_vector_typeIiLj2EEPiPS2_
    .private_segment_fixed_size: 0
    .sgpr_count:     102
    .sgpr_spill_count: 0
    .symbol:         _Z13k_bucket_sortPKiPK15HIP_vector_typeIiLj2EEPiPS2_.kd
    .uniform_work_group_size: 1
    .uses_dynamic_stack: false
    .vgpr_count:     120
    .vgpr_spill_count: 0
    .wavefront_size: 64
  - .agpr_count:     0
    .args:
      - .actual_access:  read_only
        .address_space:  global
        .offset:         0
        .size:           8
        .value_kind:     global_buffer
      - .actual_access:  read_only
        .address_space:  global
        .offset:         8
        .size:           8
        .value_kind:     global_buffer
      - .actual_access:  read_only
        .address_space:  global
        .offset:         16
        .size:           8
        .value_kind:     global_buffer
      - .actual_access:  write_only
        .address_space:  global
        .offset:         24
        .size:           8
        .value_kind:     global_buffer
      - .actual_access:  read_only
        .address_space:  global
        .offset:         32
        .size:           8
        .value_kind:     global_buffer
      - .actual_access:  read_only
        .address_space:  global
        .offset:         40
        .size:           8
        .value_kind:     global_buffer
      - .actual_access:  read_only
        .address_space:  global
        .offset:         48
        .size:           8
        .value_kind:     global_buffer
      - .actual_access:  read_only
        .address_space:  global
        .offset:         56
        .size:           8
        .value_kind:     global_buffer
      - .actual_access:  read_only
        .address_space:  global
        .offset:         64
        .size:           8
        .value_kind:     global_buffer
    .group_segment_fixed_size: 28672
    .kernarg_segment_align: 8
    .kernarg_segment_size: 72
    .language:       OpenCL C
    .language_version:
      - 2
      - 0
    .max_flat_workgroup_size: 256
    .name:           _Z5k_hopILi0EEvPKiPK15HIP_vector_typeIiLj2EEPKS2_IjLj4EEPS6_S8_S8_PKfSB_Pf
    .private_segment_fixed_size: 0
    .sgpr_count:     68
    .sgpr_spill_count: 0
    .symbol:         _Z5k_hopILi0EEvPKiPK15HIP_vector_typeIiLj2EEPKS2_IjLj4EEPS6_S8_S8_PKfSB_Pf.kd
    .uniform_work_group_size: 1
    .uses_dynamic_stack: false
    .vgpr_count:     96
    .vgpr_spill_count: 0
    .wavefront_size: 64
  - .agpr_count:     0
    .args:
      - .actual_access:  read_only
        .address_space:  global
        .offset:         0
        .size:           8
        .value_kind:     global_buffer
      - .actual_access:  read_only
        .address_space:  global
        .offset:         8
        .size:           8
        .value_kind:     global_buffer
      - .actual_access:  read_only
        .address_space:  global
        .offset:         16
        .size:           8
        .value_kind:     global_buffer
      - .actual_access:  read_only
        .address_space:  global
        .offset:         24
        .size:           8
        .value_kind:     global_buffer
      - .actual_access:  read_only
        .address_space:  global
        .offset:         32
        .size:           8
        .value_kind:     global_buffer
      - .actual_access:  read_only
        .address_space:  global
        .offset:         40
        .size:           8
        .value_kind:     global_buffer
      - .actual_access:  read_only
        .address_space:  global
        .offset:         48
        .size:           8
        .value_kind:     global_buffer
      - .actual_access:  read_only
        .address_space:  global
        .offset:         56
        .size:           8
        .value_kind:     global_buffer
      - .actual_access:  write_only
        .address_space:  global
        .offset:         64
        .size:           8
        .value_kind:     global_buffer
    .group_segment_fixed_size: 28672
    .kernarg_segment_align: 8
    .kernarg_segment_size: 72
    .language:       OpenCL C
    .language_version:
      - 2
      - 0
    .max_flat_workgroup_size: 256
    .name:           _Z5k_hopILi1EEvPKiPK15HIP_vector_typeIiLj2EEPKS2_IjLj4EEPS6_S8_S8_PKfSB_Pf
    .private_segment_fixed_size: 0
    .sgpr_count:     68
    .sgpr_spill_count: 0
    .symbol:         _Z5k_hopILi1EEvPKiPK15HIP_vector_typeIiLj2EEPKS2_IjLj4EEPS6_S8_S8_PKfSB_Pf.kd
    .uniform_work_group_size: 1
    .uses_dynamic_stack: false
    .vgpr_count:     96
    .vgpr_spill_count: 0
    .wavefront_size: 64
